# dense attention epilogue: output tile staged through a free LDS ring slot, full-line dwordx4 stores instead of byte stores; router-bias dot products with 32 loads in flight
# baseline (speedup 1.0000x reference)
.LBB0_98:
	v_lshl_add_u64 v[30:31], s[16:17], 0, v[16:17]
	v_lshl_add_u64 v[32:33], s[16:17], 0, v[14:15]
	global_load_dword v48, v[30:31], off
	global_load_dword v49, v[32:33], off
	v_lshl_add_u64 v[34:35], s[16:17], 0, v[12:13]
	v_lshl_add_u64 v[36:37], s[16:17], 0, v[10:11]
	global_load_dword v50, v[34:35], off
	global_load_dword v51, v[36:37], off
	v_add_u32_e32 v29, s7, v28
	v_lshl_add_u64 v[38:39], s[16:17], 0, v[8:9]
	v_lshl_add_u64 v[40:41], s[16:17], 0, v[6:7]
	v_lshl_add_u64 v[42:43], s[16:17], 0, v[4:5]
	v_add_u32_e32 v46, 0x1a00, v29
	global_load_dword v52, v[38:39], off
	global_load_dword v53, v[40:41], off
	global_load_dword v54, v[42:43], off
	v_lshl_add_u64 v[44:45], s[16:17], 0, v[2:3]
	v_add_u32_e32 v30, 0x1a40, v29
	v_add_u32_e32 v32, 0x1a80, v29
	v_add_u32_e32 v34, 0x1ac0, v29
	v_add_u32_e32 v36, 0x1b00, v29
	v_add_u32_e32 v38, 0x1b40, v29
	v_add_u32_e32 v40, 0x1b80, v29
	v_add_u32_e32 v42, 0x1bc0, v29
	v_ashrrev_i32_e32 v47, 31, v46
	global_load_dword v29, v[44:45], off
	v_ashrrev_i32_e32 v31, 31, v30
	v_ashrrev_i32_e32 v33, 31, v32
	v_ashrrev_i32_e32 v35, 31, v34
	v_ashrrev_i32_e32 v37, 31, v36
	v_ashrrev_i32_e32 v39, 31, v38
	v_ashrrev_i32_e32 v41, 31, v40
	v_ashrrev_i32_e32 v43, 31, v42
	v_lshl_add_u64 v[44:45], v[46:47], 2, s[10:11]
	v_lshl_add_u64 v[30:31], v[30:31], 2, s[10:11]
	v_lshl_add_u64 v[32:33], v[32:33], 2, s[10:11]
	v_lshl_add_u64 v[34:35], v[34:35], 2, s[10:11]
	v_lshl_add_u64 v[36:37], v[36:37], 2, s[10:11]
	v_lshl_add_u64 v[38:39], v[38:39], 2, s[10:11]
	v_lshl_add_u64 v[40:41], v[40:41], 2, s[10:11]
	v_lshl_add_u64 v[42:43], v[42:43], 2, s[10:11]
	global_load_dword v46, v[44:45], off
	global_load_dword v47, v[30:31], off
	global_load_dword v55, v[32:33], off
	global_load_dword v56, v[34:35], off
	global_load_dword v57, v[36:37], off
	global_load_dword v58, v[38:39], off
	global_load_dword v59, v[40:41], off
	global_load_dword v60, v[42:43], off
	v_add_u32_e32 v28, 0x200, v28
	s_add_u32 s16, s16, 0x20000
	s_addc_u32 s17, s17, 0
	v_lshl_add_u64 v[102:103], s[16:17], 0, v[16:17]
	v_lshl_add_u64 v[104:105], s[16:17], 0, v[14:15]
	global_load_dword v120, v[102:103], off
	global_load_dword v121, v[104:105], off
	v_lshl_add_u64 v[106:107], s[16:17], 0, v[12:13]
	v_lshl_add_u64 v[108:109], s[16:17], 0, v[10:11]
	global_load_dword v122, v[106:107], off
	global_load_dword v123, v[108:109], off
	v_add_u32_e32 v101, s7, v28
	v_lshl_add_u64 v[110:111], s[16:17], 0, v[8:9]
	v_lshl_add_u64 v[112:113], s[16:17], 0, v[6:7]
	v_lshl_add_u64 v[114:115], s[16:17], 0, v[4:5]
	v_add_u32_e32 v118, 0x1a00, v101
	global_load_dword v124, v[110:111], off
	global_load_dword v125, v[112:113], off
	global_load_dword v126, v[114:115], off
	v_lshl_add_u64 v[116:117], s[16:17], 0, v[2:3]
	v_add_u32_e32 v102, 0x1a40, v101
	v_add_u32_e32 v104, 0x1a80, v101
	v_add_u32_e32 v106, 0x1ac0, v101
	v_add_u32_e32 v108, 0x1b00, v101
	v_add_u32_e32 v110, 0x1b40, v101
	v_add_u32_e32 v112, 0x1b80, v101
	v_add_u32_e32 v114, 0x1bc0, v101
	v_ashrrev_i32_e32 v119, 31, v118
	global_load_dword v101, v[116:117], off
	v_ashrrev_i32_e32 v103, 31, v102
	v_ashrrev_i32_e32 v105, 31, v104
	v_ashrrev_i32_e32 v107, 31, v106
	v_ashrrev_i32_e32 v109, 31, v108
	v_ashrrev_i32_e32 v111, 31, v110
	v_ashrrev_i32_e32 v113, 31, v112
	v_ashrrev_i32_e32 v115, 31, v114
	v_lshl_add_u64 v[116:117], v[118:119], 2, s[10:11]
	v_lshl_add_u64 v[102:103], v[102:103], 2, s[10:11]
	v_lshl_add_u64 v[104:105], v[104:105], 2, s[10:11]
	v_lshl_add_u64 v[106:107], v[106:107], 2, s[10:11]
	v_lshl_add_u64 v[108:109], v[108:109], 2, s[10:11]
	v_lshl_add_u64 v[110:111], v[110:111], 2, s[10:11]
	v_lshl_add_u64 v[112:113], v[112:113], 2, s[10:11]
	v_lshl_add_u64 v[114:115], v[114:115], 2, s[10:11]
	global_load_dword v118, v[116:117], off
	global_load_dword v119, v[102:103], off
	global_load_dword v127, v[104:105], off
	global_load_dword v128, v[106:107], off
	global_load_dword v129, v[108:109], off
	global_load_dword v130, v[110:111], off
	global_load_dword v131, v[112:113], off
	global_load_dword v132, v[114:115], off
	v_add_u32_e32 v28, 0x200, v28
	s_add_u32 s16, s16, 0x20000
	s_addc_u32 s17, s17, 0
	v_cmp_lt_u32_e64 s[0:1], s21, v28
	s_or_b64 s[8:9], s[0:1], s[8:9]
	s_waitcnt vmcnt(23)
	v_fmac_f32_e32 v27, v46, v48
	s_waitcnt vmcnt(22)
	v_fmac_f32_e32 v27, v47, v49
	s_waitcnt vmcnt(21)
	v_fmac_f32_e32 v27, v55, v50
	s_waitcnt vmcnt(20)
	v_fmac_f32_e32 v27, v56, v51
	s_waitcnt vmcnt(19)
	v_fmac_f32_e32 v27, v57, v52
	s_waitcnt vmcnt(18)
	v_fmac_f32_e32 v27, v58, v53
	s_waitcnt vmcnt(17)
	v_fmac_f32_e32 v27, v59, v54
	s_waitcnt vmcnt(16)
	v_fmac_f32_e32 v27, v60, v29
	s_waitcnt vmcnt(7)
	v_fmac_f32_e32 v27, v118, v120
	s_waitcnt vmcnt(6)
	v_fmac_f32_e32 v27, v119, v121
	s_waitcnt vmcnt(5)
	v_fmac_f32_e32 v27, v127, v122
	s_waitcnt vmcnt(4)
	v_fmac_f32_e32 v27, v128, v123
	s_waitcnt vmcnt(3)
	v_fmac_f32_e32 v27, v129, v124
	s_waitcnt vmcnt(2)
	v_fmac_f32_e32 v27, v130, v125
	s_waitcnt vmcnt(1)
	v_fmac_f32_e32 v27, v131, v126
	s_waitcnt vmcnt(0)
	v_fmac_f32_e32 v27, v132, v101
	s_andn2_b64 exec, exec, s[8:9]
	s_cbranch_execnz .LBB0_98
	s_or_b64 exec, exec, s[8:9]
	ds_swizzle_b32 v2, v27 offset:swizzle(SWAP,1)
	s_waitcnt lgkmcnt(0)
	v_add_f32_e32 v2, v27, v2
	ds_swizzle_b32 v4, v2 offset:swizzle(SWAP,2)
	s_waitcnt lgkmcnt(0)
	v_add_f32_e32 v2, v2, v4
	ds_swizzle_b32 v4, v2 offset:swizzle(SWAP,4)
	s_waitcnt lgkmcnt(0)
	v_add_f32_e32 v2, v2, v4
	ds_swizzle_b32 v4, v2 offset:swizzle(SWAP,8)
	s_waitcnt lgkmcnt(0)
	v_add_f32_e32 v2, v2, v4
	ds_swizzle_b32 v4, v2 offset:swizzle(SWAP,16)
	s_waitcnt lgkmcnt(0)
	v_add_f32_e32 v2, v2, v4
	v_mov_b32_e32 v4, v2
	s_nop 1
	v_permlane32_swap_b32_e32 v2, v4
	s_and_saveexec_b64 s[0:1], vcc
	s_cbranch_execz .LBB0_96
	s_ashr_i32 s7, s6, 31
	s_lshl_b64 s[8:9], s[6:7], 2
	s_add_u32 s8, s18, s8
	s_addc_u32 s9, s19, s9
	v_add_f32_e32 v2, v2, v4
	global_store_dword v3, v2, s[8:9]
	s_branch .LBB0_96

.LBB0_386:
	s_or_b64 exec, exec, s[4:5]
	s_waitcnt lgkmcnt(0)
	s_barrier
	v_add_u32_e32 v2, v135, v185
	ds_read_b128 v[68:71], v2
	ds_read_b128 v[72:75], v2 offset:32
	ds_read_b128 v[76:79], v2 offset:64
	ds_read_b128 v[80:83], v2 offset:96
	s_or_b32 s4, s14, s13
	s_mul_hi_i32 s5, s4, 0xa00
	s_mulk_i32 s4, 0xa00
	s_add_u32 s4, s18, s4
	s_addc_u32 s5, s19, s5
	s_add_u32 s4, s4, s12
	s_addc_u32 s5, s5, 0
	v_lshrrev_b32_e32 v84, 6, v1
	v_and_b32_e32 v85, 1, v84
	v_lshrrev_b32_e32 v84, 1, v84
	v_lshlrev_b32_e32 v84, 14, v84
	v_lshl_add_u32 v84, v85, 12, v84
	v_add_u32_e32 v84, 0x2000, v84
	v_and_b32_e32 v85, 31, v1
	v_and_b32_e32 v86, 32, v1
	v_lshl_add_u32 v85, v86, 4, v85
	v_add_u32_e32 v85, v84, v85
	v_and_b32_e32 v86, 63, v1
	v_lshrrev_b32_e32 v87, 3, v86
	v_and_b32_e32 v86, 7, v86
	v_lshlrev_b32_e32 v86, 4, v86
	v_lshl_add_u32 v88, v87, 7, v86
	v_add_u32_e32 v88, v84, v88
	v_lshrrev_b32_e32 v89, 6, v1
	v_lshl_add_u32 v89, v89, 5, v87
	v_mul_u32_u24_e32 v89, 0xa00, v89
	v_add_u32_e32 v90, v89, v86
	v_mov_b32_e32 v91, v3
	v_lshl_add_u64 v[90:91], s[4:5], 0, v[90:91]
	v_lshl_add_u64 v[90:91], v[90:91], 0, s[30:31]
	s_mov_b64 s[74:75], 0x5000
	s_waitcnt lgkmcnt(0)
	v_rcp_f32_e32 v116, v68
	v_rcp_f32_e32 v117, v69
	v_rcp_f32_e32 v118, v70
	v_rcp_f32_e32 v119, v71
	v_rcp_f32_e32 v120, v72
	v_rcp_f32_e32 v121, v73
	v_rcp_f32_e32 v122, v74
	v_rcp_f32_e32 v123, v75
	v_rcp_f32_e32 v124, v76
	v_rcp_f32_e32 v125, v77
	v_rcp_f32_e32 v126, v78
	v_rcp_f32_e32 v127, v79
	v_rcp_f32_e32 v128, v80
	v_rcp_f32_e32 v129, v81
	v_rcp_f32_e32 v130, v82
	v_rcp_f32_e32 v131, v83
	v_mul_f32_e32 v116, 0x43000000, v116
	v_mul_f32_e32 v117, 0x43000000, v117
	v_mul_f32_e32 v118, 0x43000000, v118
	v_mul_f32_e32 v119, 0x43000000, v119
	v_mul_f32_e32 v120, 0x43000000, v120
	v_mul_f32_e32 v121, 0x43000000, v121
	v_mul_f32_e32 v122, 0x43000000, v122
	v_mul_f32_e32 v123, 0x43000000, v123
	v_mul_f32_e32 v124, 0x43000000, v124
	v_mul_f32_e32 v125, 0x43000000, v125
	v_mul_f32_e32 v126, 0x43000000, v126
	v_mul_f32_e32 v127, 0x43000000, v127
	v_mul_f32_e32 v128, 0x43000000, v128
	v_mul_f32_e32 v129, 0x43000000, v129
	v_mul_f32_e32 v130, 0x43000000, v130
	v_mul_f32_e32 v131, 0x43000000, v131
	v_mul_f32_e32 v92, v52, v116
	v_mul_f32_e32 v93, v36, v116
	v_mul_f32_e32 v94, v20, v116
	v_mul_f32_e32 v95, v4, v116
	v_med3_f32 v92, v92, s58, v199
	v_med3_f32 v93, v93, s58, v199
	v_med3_f32 v94, v94, s58, v199
	v_med3_f32 v95, v95, s58, v199
	v_cvt_pk_fp8_f32 v96, v92, v93
	v_cvt_pk_fp8_f32 v97, v94, v95
	ds_write_b8 v85, v96
	v_lshrrev_b32_e32 v98, 8, v96
	ds_write_b8 v85, v98 offset:32
	ds_write_b8 v85, v97 offset:64
	v_lshrrev_b32_e32 v99, 8, v97
	ds_write_b8 v85, v99 offset:96
	v_mul_f32_e32 v100, v53, v117
	v_mul_f32_e32 v101, v37, v117
	v_mul_f32_e32 v102, v21, v117
	v_mul_f32_e32 v103, v5, v117
	v_med3_f32 v100, v100, s58, v199
	v_med3_f32 v101, v101, s58, v199
	v_med3_f32 v102, v102, s58, v199
	v_med3_f32 v103, v103, s58, v199
	v_cvt_pk_fp8_f32 v104, v100, v101
	v_cvt_pk_fp8_f32 v105, v102, v103
	ds_write_b8 v85, v104 offset:128
	v_lshrrev_b32_e32 v106, 8, v104
	ds_write_b8 v85, v106 offset:160
	ds_write_b8 v85, v105 offset:192
	v_lshrrev_b32_e32 v107, 8, v105
	ds_write_b8 v85, v107 offset:224
	v_mul_f32_e32 v92, v54, v118
	v_mul_f32_e32 v93, v38, v118
	v_mul_f32_e32 v94, v22, v118
	v_mul_f32_e32 v95, v6, v118
	v_med3_f32 v92, v92, s58, v199
	v_med3_f32 v93, v93, s58, v199
	v_med3_f32 v94, v94, s58, v199
	v_med3_f32 v95, v95, s58, v199
	v_cvt_pk_fp8_f32 v96, v92, v93
	v_cvt_pk_fp8_f32 v97, v94, v95
	ds_write_b8 v85, v96 offset:256
	v_lshrrev_b32_e32 v98, 8, v96
	ds_write_b8 v85, v98 offset:288
	ds_write_b8 v85, v97 offset:320
	v_lshrrev_b32_e32 v99, 8, v97
	ds_write_b8 v85, v99 offset:352
	v_mul_f32_e32 v100, v55, v119
	v_mul_f32_e32 v101, v39, v119
	v_mul_f32_e32 v102, v23, v119
	v_mul_f32_e32 v103, v7, v119
	v_med3_f32 v100, v100, s58, v199
	v_med3_f32 v101, v101, s58, v199
	v_med3_f32 v102, v102, s58, v199
	v_med3_f32 v103, v103, s58, v199
	v_cvt_pk_fp8_f32 v104, v100, v101
	v_cvt_pk_fp8_f32 v105, v102, v103
	ds_write_b8 v85, v104 offset:384
	v_lshrrev_b32_e32 v106, 8, v104
	ds_write_b8 v85, v106 offset:416
	ds_write_b8 v85, v105 offset:448
	v_lshrrev_b32_e32 v107, 8, v105
	ds_write_b8 v85, v107 offset:480
	v_mul_f32_e32 v92, v56, v120
	v_mul_f32_e32 v93, v40, v120
	v_mul_f32_e32 v94, v24, v120
	v_mul_f32_e32 v95, v8, v120
	v_med3_f32 v92, v92, s58, v199
	v_med3_f32 v93, v93, s58, v199
	v_med3_f32 v94, v94, s58, v199
	v_med3_f32 v95, v95, s58, v199
	v_cvt_pk_fp8_f32 v96, v92, v93
	v_cvt_pk_fp8_f32 v97, v94, v95
	ds_write_b8 v85, v96 offset:1024
	v_lshrrev_b32_e32 v98, 8, v96
	ds_write_b8 v85, v98 offset:1056
	ds_write_b8 v85, v97 offset:1088
	v_lshrrev_b32_e32 v99, 8, v97
	ds_write_b8 v85, v99 offset:1120
	v_mul_f32_e32 v100, v57, v121
	v_mul_f32_e32 v101, v41, v121
	v_mul_f32_e32 v102, v25, v121
	v_mul_f32_e32 v103, v9, v121
	v_med3_f32 v100, v100, s58, v199
	v_med3_f32 v101, v101, s58, v199
	v_med3_f32 v102, v102, s58, v199
	v_med3_f32 v103, v103, s58, v199
	v_cvt_pk_fp8_f32 v104, v100, v101
	v_cvt_pk_fp8_f32 v105, v102, v103
	ds_write_b8 v85, v104 offset:1152
	v_lshrrev_b32_e32 v106, 8, v104
	ds_write_b8 v85, v106 offset:1184
	ds_write_b8 v85, v105 offset:1216
	v_lshrrev_b32_e32 v107, 8, v105
	ds_write_b8 v85, v107 offset:1248
	v_mul_f32_e32 v92, v58, v122
	v_mul_f32_e32 v93, v42, v122
	v_mul_f32_e32 v94, v26, v122
	v_mul_f32_e32 v95, v10, v122
	v_med3_f32 v92, v92, s58, v199
	v_med3_f32 v93, v93, s58, v199
	v_med3_f32 v94, v94, s58, v199
	v_med3_f32 v95, v95, s58, v199
	v_cvt_pk_fp8_f32 v96, v92, v93
	v_cvt_pk_fp8_f32 v97, v94, v95
	ds_write_b8 v85, v96 offset:1280
	v_lshrrev_b32_e32 v98, 8, v96
	ds_write_b8 v85, v98 offset:1312
	ds_write_b8 v85, v97 offset:1344
	v_lshrrev_b32_e32 v99, 8, v97
	ds_write_b8 v85, v99 offset:1376
	v_mul_f32_e32 v100, v59, v123
	v_mul_f32_e32 v101, v43, v123
	v_mul_f32_e32 v102, v27, v123
	v_mul_f32_e32 v103, v11, v123
	v_med3_f32 v100, v100, s58, v199
	v_med3_f32 v101, v101, s58, v199
	v_med3_f32 v102, v102, s58, v199
	v_med3_f32 v103, v103, s58, v199
	v_cvt_pk_fp8_f32 v104, v100, v101
	v_cvt_pk_fp8_f32 v105, v102, v103
	ds_write_b8 v85, v104 offset:1408
	v_lshrrev_b32_e32 v106, 8, v104
	ds_write_b8 v85, v106 offset:1440
	ds_write_b8 v85, v105 offset:1472
	v_lshrrev_b32_e32 v107, 8, v105
	ds_write_b8 v85, v107 offset:1504
	v_mul_f32_e32 v92, v60, v124
	v_mul_f32_e32 v93, v44, v124
	v_mul_f32_e32 v94, v28, v124
	v_mul_f32_e32 v95, v12, v124
	v_med3_f32 v92, v92, s58, v199
	v_med3_f32 v93, v93, s58, v199
	v_med3_f32 v94, v94, s58, v199
	v_med3_f32 v95, v95, s58, v199
	v_cvt_pk_fp8_f32 v96, v92, v93
	v_cvt_pk_fp8_f32 v97, v94, v95
	ds_write_b8 v85, v96 offset:2048
	v_lshrrev_b32_e32 v98, 8, v96
	ds_write_b8 v85, v98 offset:2080
	ds_write_b8 v85, v97 offset:2112
	v_lshrrev_b32_e32 v99, 8, v97
	ds_write_b8 v85, v99 offset:2144
	v_mul_f32_e32 v100, v61, v125
	v_mul_f32_e32 v101, v45, v125
	v_mul_f32_e32 v102, v29, v125
	v_mul_f32_e32 v103, v13, v125
	v_med3_f32 v100, v100, s58, v199
	v_med3_f32 v101, v101, s58, v199
	v_med3_f32 v102, v102, s58, v199
	v_med3_f32 v103, v103, s58, v199
	v_cvt_pk_fp8_f32 v104, v100, v101
	v_cvt_pk_fp8_f32 v105, v102, v103
	ds_write_b8 v85, v104 offset:2176
	v_lshrrev_b32_e32 v106, 8, v104
	ds_write_b8 v85, v106 offset:2208
	ds_write_b8 v85, v105 offset:2240
	v_lshrrev_b32_e32 v107, 8, v105
	ds_write_b8 v85, v107 offset:2272
	v_mul_f32_e32 v92, v62, v126
	v_mul_f32_e32 v93, v46, v126
	v_mul_f32_e32 v94, v30, v126
	v_mul_f32_e32 v95, v14, v126
	v_med3_f32 v92, v92, s58, v199
	v_med3_f32 v93, v93, s58, v199
	v_med3_f32 v94, v94, s58, v199
	v_med3_f32 v95, v95, s58, v199
	v_cvt_pk_fp8_f32 v96, v92, v93
	v_cvt_pk_fp8_f32 v97, v94, v95
	ds_write_b8 v85, v96 offset:2304
	v_lshrrev_b32_e32 v98, 8, v96
	ds_write_b8 v85, v98 offset:2336
	ds_write_b8 v85, v97 offset:2368
	v_lshrrev_b32_e32 v99, 8, v97
	ds_write_b8 v85, v99 offset:2400
	v_mul_f32_e32 v100, v63, v127
	v_mul_f32_e32 v101, v47, v127
	v_mul_f32_e32 v102, v31, v127
	v_mul_f32_e32 v103, v15, v127
	v_med3_f32 v100, v100, s58, v199
	v_med3_f32 v101, v101, s58, v199
	v_med3_f32 v102, v102, s58, v199
	v_med3_f32 v103, v103, s58, v199
	v_cvt_pk_fp8_f32 v104, v100, v101
	v_cvt_pk_fp8_f32 v105, v102, v103
	ds_write_b8 v85, v104 offset:2432
	v_lshrrev_b32_e32 v106, 8, v104
	ds_write_b8 v85, v106 offset:2464
	ds_write_b8 v85, v105 offset:2496
	v_lshrrev_b32_e32 v107, 8, v105
	ds_write_b8 v85, v107 offset:2528
	v_mul_f32_e32 v92, v64, v128
	v_mul_f32_e32 v93, v48, v128
	v_mul_f32_e32 v94, v32, v128
	v_mul_f32_e32 v95, v16, v128
	v_med3_f32 v92, v92, s58, v199
	v_med3_f32 v93, v93, s58, v199
	v_med3_f32 v94, v94, s58, v199
	v_med3_f32 v95, v95, s58, v199
	v_cvt_pk_fp8_f32 v96, v92, v93
	v_cvt_pk_fp8_f32 v97, v94, v95
	ds_write_b8 v85, v96 offset:3072
	v_lshrrev_b32_e32 v98, 8, v96
	ds_write_b8 v85, v98 offset:3104
	ds_write_b8 v85, v97 offset:3136
	v_lshrrev_b32_e32 v99, 8, v97
	ds_write_b8 v85, v99 offset:3168
	v_mul_f32_e32 v100, v65, v129
	v_mul_f32_e32 v101, v49, v129
	v_mul_f32_e32 v102, v33, v129
	v_mul_f32_e32 v103, v17, v129
	v_med3_f32 v100, v100, s58, v199
	v_med3_f32 v101, v101, s58, v199
	v_med3_f32 v102, v102, s58, v199
	v_med3_f32 v103, v103, s58, v199
	v_cvt_pk_fp8_f32 v104, v100, v101
	v_cvt_pk_fp8_f32 v105, v102, v103
	ds_write_b8 v85, v104 offset:3200
	v_lshrrev_b32_e32 v106, 8, v104
	ds_write_b8 v85, v106 offset:3232
	ds_write_b8 v85, v105 offset:3264
	v_lshrrev_b32_e32 v107, 8, v105
	ds_write_b8 v85, v107 offset:3296
	v_mul_f32_e32 v92, v66, v130
	v_mul_f32_e32 v93, v50, v130
	v_mul_f32_e32 v94, v34, v130
	v_mul_f32_e32 v95, v18, v130
	v_med3_f32 v92, v92, s58, v199
	v_med3_f32 v93, v93, s58, v199
	v_med3_f32 v94, v94, s58, v199
	v_med3_f32 v95, v95, s58, v199
	v_cvt_pk_fp8_f32 v96, v92, v93
	v_cvt_pk_fp8_f32 v97, v94, v95
	ds_write_b8 v85, v96 offset:3328
	v_lshrrev_b32_e32 v98, 8, v96
	ds_write_b8 v85, v98 offset:3360
	ds_write_b8 v85, v97 offset:3392
	v_lshrrev_b32_e32 v99, 8, v97
	ds_write_b8 v85, v99 offset:3424
	v_mul_f32_e32 v100, v67, v131
	v_mul_f32_e32 v101, v51, v131
	v_mul_f32_e32 v102, v35, v131
	v_mul_f32_e32 v103, v19, v131
	v_med3_f32 v100, v100, s58, v199
	v_med3_f32 v101, v101, s58, v199
	v_med3_f32 v102, v102, s58, v199
	v_med3_f32 v103, v103, s58, v199
	v_cvt_pk_fp8_f32 v104, v100, v101
	v_cvt_pk_fp8_f32 v105, v102, v103
	ds_write_b8 v85, v104 offset:3456
	v_lshrrev_b32_e32 v106, 8, v104
	ds_write_b8 v85, v106 offset:3488
	ds_write_b8 v85, v105 offset:3520
	v_lshrrev_b32_e32 v107, 8, v105
	ds_write_b8 v85, v107 offset:3552
	s_waitcnt lgkmcnt(0)
	ds_read_b128 v[108:111], v88
	ds_read_b128 v[112:115], v88 offset:1024
	ds_read_b128 v[68:71], v88 offset:2048
	ds_read_b128 v[72:75], v88 offset:3072
	s_waitcnt lgkmcnt(3)
	global_store_dwordx4 v[90:91], v[108:111], off
	v_lshl_add_u64 v[76:77], v[90:91], 0, s[74:75]
	s_waitcnt lgkmcnt(2)
	global_store_dwordx4 v[76:77], v[112:115], off
	v_lshl_add_u64 v[78:79], v[76:77], 0, s[74:75]
	s_waitcnt lgkmcnt(1)
	global_store_dwordx4 v[78:79], v[68:71], off
	v_lshl_add_u64 v[80:81], v[78:79], 0, s[74:75]
	s_waitcnt lgkmcnt(0)
	global_store_dwordx4 v[80:81], v[72:75], off
	s_add_i32 s72, s72, s33
	s_add_i32 s71, s71, 1
	s_cmpk_lt_i32 s72, 0x200
	s_cbranch_scc0 .LBB0_427
